# bundle1 + 64B alignment of hot loop headers (P2/P8/P9 K-loops, retention chunk loop, P10 token loop)
# speedup vs baseline: 1.0111x; 1.0063x over previous
; #define G8_STAGE(bufoff, gbase, voff) do { _Pragma("unroll") for (int _i = 0; _i < 2; ++_i) \
;         __builtin_amdgcn_global_load_lds((const unsigned*)((const char*)(gbase) + (voff)[_i]), (LAS unsigned*)(lds + (bufoff) + ldsw + _i * 8192), 16, 0, 0); } while (0)
; #define G8_LDA(dst, b, h) do { _Pragma("unroll") for (int m = 0; m < 4; ++m) _Pragma("unroll") for (int k = 0; k < 2; ++k) dst[m][k] = *(const LAS bf16x8*)(lds + G8_SA(b, h) + aoff + m * 2048 + k * 1024); } while (0)
; #define G8_LDB(dst, b, h) do { _Pragma("unroll") for (int n = 0; n < 2; ++n) _Pragma("unroll") for (int k = 0; k < 2; ++k) dst[n][k] = *(const LAS bf16x8*)(lds + G8_SB(b, h) + boff + n * 2048 + k * 1024); } while (0)
; #define G8_WAIT_V(n) asm volatile("s_waitcnt vmcnt(" #n ")" ::: "memory")
; #define G8_WAIT_L(n) asm volatile("s_waitcnt lgkmcnt(" #n ")" ::: "memory")
; #define G8_BAR __builtin_amdgcn_s_barrier()
; #define G8_SCHED __builtin_amdgcn_sched_barrier(0)
; template <class Epi, class Sched, int NT, bool F8 = false>
; __device__ __forceinline__ void gemm_phase(LAS unsigned char* lds, const Sched& S, const Epi& E) {
;     ...
;             G8_WAIT_VF(t, ui); G8_WAIT_L(0); G8_BAR; G8_MMA(1, 0, At, B0); G8_MMA(1, 1, At, B1); G8_BAR; G8_SCHED;
;             G8_LDB(B0, 1, 0); G8_LDB(B1, 1, 1); G8_SCHED; G8_LDA(At, 1, 0); G8_STAGE(G8_SA(0, 1), a2, cur.vA1);
;             G8_WAIT_V(8); G8_WAIT_L(0); G8_BAR; G8_MMA(0, 0, At, B0); G8_MMA(0, 1, At, B1); G8_BAR; G8_SCHED;
.Lg8e1:
	s_waitcnt lgkmcnt(0)
	s_barrier
	s_setprio 1
	s_waitcnt lgkmcnt(0)
	v_mfma_f32_16x16x32_bf16 v[62:65], v[146:149], v[162:165], v[62:65]
	v_mfma_f32_16x16x32_bf16 v[58:61], v[154:157], v[162:165], v[58:61]
	v_mfma_f32_16x16x32_bf16 v[54:57], v[146:149], v[170:173], v[54:57]
	v_mfma_f32_16x16x32_bf16 v[50:53], v[154:157], v[170:173], v[50:53]
	v_mfma_f32_16x16x32_bf16 v[38:41], v[146:149], v[178:181], v[38:41]
	v_mfma_f32_16x16x32_bf16 v[34:37], v[154:157], v[178:181], v[34:37]
	v_mfma_f32_16x16x32_bf16 v[22:25], v[146:149], v[186:189], v[22:25]
	v_mfma_f32_16x16x32_bf16 v[18:21], v[154:157], v[186:189], v[18:21]
	v_mfma_f32_16x16x32_bf16 v[62:65], v[150:153], v[166:169], v[62:65]
	v_mfma_f32_16x16x32_bf16 v[58:61], v[158:161], v[166:169], v[58:61]
	v_mfma_f32_16x16x32_bf16 v[54:57], v[150:153], v[174:177], v[54:57]
	v_mfma_f32_16x16x32_bf16 v[50:53], v[158:161], v[174:177], v[50:53]
	v_mfma_f32_16x16x32_bf16 v[38:41], v[150:153], v[182:185], v[38:41]
	v_mfma_f32_16x16x32_bf16 v[34:37], v[158:161], v[182:185], v[34:37]
	v_mfma_f32_16x16x32_bf16 v[22:25], v[150:153], v[190:193], v[22:25]
	v_mfma_f32_16x16x32_bf16 v[18:21], v[158:161], v[190:193], v[18:21]
	s_setprio 0
	s_setprio 1
	v_mfma_f32_16x16x32_bf16 v[46:49], v[130:133], v[162:165], v[46:49]
	v_mfma_f32_16x16x32_bf16 v[42:45], v[138:141], v[162:165], v[42:45]
	v_mfma_f32_16x16x32_bf16 v[30:33], v[130:133], v[170:173], v[30:33]
	v_mfma_f32_16x16x32_bf16 v[26:29], v[138:141], v[170:173], v[26:29]
	v_mfma_f32_16x16x32_bf16 v[14:17], v[130:133], v[178:181], v[14:17]
	v_mfma_f32_16x16x32_bf16 v[10:13], v[138:141], v[178:181], v[10:13]
	v_mfma_f32_16x16x32_bf16 v[6:9], v[130:133], v[186:189], v[6:9]
	v_mfma_f32_16x16x32_bf16 v[2:5], v[138:141], v[186:189], v[2:5]
	v_mfma_f32_16x16x32_bf16 v[46:49], v[134:137], v[166:169], v[46:49]
	v_mfma_f32_16x16x32_bf16 v[42:45], v[142:145], v[166:169], v[42:45]
	v_mfma_f32_16x16x32_bf16 v[30:33], v[134:137], v[174:177], v[30:33]
	v_mfma_f32_16x16x32_bf16 v[26:29], v[142:145], v[174:177], v[26:29]
	v_mfma_f32_16x16x32_bf16 v[14:17], v[134:137], v[182:185], v[14:17]
	v_mfma_f32_16x16x32_bf16 v[10:13], v[142:145], v[182:185], v[10:13]
	v_mfma_f32_16x16x32_bf16 v[6:9], v[134:137], v[190:193], v[6:9]
	v_mfma_f32_16x16x32_bf16 v[2:5], v[142:145], v[190:193], v[2:5]
	s_setprio 0
	s_barrier
	v_add_u32_e32 v142, s46, v209
	v_add_u32_e32 v158, s47, v209
	ds_read_b128 v[130:133], v142
	ds_read_b128 v[134:137], v142 offset:1024
	ds_read_b128 v[138:141], v142 offset:2048
	ds_read_b128 v[142:145], v142 offset:3072
	ds_read_b128 v[146:149], v158
	ds_read_b128 v[150:153], v158 offset:1024
	ds_read_b128 v[154:157], v158 offset:2048
	ds_read_b128 v[158:161], v158 offset:3072
	s_mov_b32 m0, s41
	v_lshl_add_u64 v[228:229], s[24:25], 0, v[228:229]
	ds_read_b128 v[162:165], v236 offset:32768
	ds_read_b128 v[166:169], v236 offset:33792
	ds_read_b128 v[170:173], v236 offset:34816
	ds_read_b128 v[174:177], v236 offset:35840
	ds_read_b128 v[178:181], v236 offset:36864
	ds_read_b128 v[182:185], v236 offset:37888
	ds_read_b128 v[186:189], v236 offset:38912
	ds_read_b128 v[190:193], v236 offset:39936
	global_load_lds_dwordx4 v[228:229], off
	v_lshl_add_u64 v[226:227], s[24:25], 0, v[226:227]
	s_mov_b32 m0, s42
	s_nop 0
	global_load_lds_dwordx4 v[226:227], off
	s_waitcnt vmcnt(8)
	s_waitcnt lgkmcnt(0)
	s_barrier
	s_setprio 1
	s_waitcnt lgkmcnt(0)
	v_mfma_f32_16x16x32_bf16 v[126:129], v[130:133], v[162:165], v[126:129]
	v_mfma_f32_16x16x32_bf16 v[122:125], v[138:141], v[162:165], v[122:125]
	v_mfma_f32_16x16x32_bf16 v[118:121], v[130:133], v[170:173], v[118:121]
	v_mfma_f32_16x16x32_bf16 v[114:117], v[138:141], v[170:173], v[114:117]
	v_mfma_f32_16x16x32_bf16 v[102:105], v[130:133], v[178:181], v[102:105]
	v_mfma_f32_16x16x32_bf16 v[98:101], v[138:141], v[178:181], v[98:101]
	v_mfma_f32_16x16x32_bf16 v[86:89], v[130:133], v[186:189], v[86:89]
	v_mfma_f32_16x16x32_bf16 v[82:85], v[138:141], v[186:189], v[82:85]
	v_mfma_f32_16x16x32_bf16 v[126:129], v[134:137], v[166:169], v[126:129]
	v_mfma_f32_16x16x32_bf16 v[122:125], v[142:145], v[166:169], v[122:125]
	v_mfma_f32_16x16x32_bf16 v[118:121], v[134:137], v[174:177], v[118:121]
	v_mfma_f32_16x16x32_bf16 v[114:117], v[142:145], v[174:177], v[114:117]
	v_mfma_f32_16x16x32_bf16 v[102:105], v[134:137], v[182:185], v[102:105]
	v_mfma_f32_16x16x32_bf16 v[98:101], v[142:145], v[182:185], v[98:101]
	v_mfma_f32_16x16x32_bf16 v[86:89], v[134:137], v[190:193], v[86:89]
	v_mfma_f32_16x16x32_bf16 v[82:85], v[142:145], v[190:193], v[82:85]
	s_setprio 0
	s_setprio 1
	v_mfma_f32_16x16x32_bf16 v[110:113], v[146:149], v[162:165], v[110:113]
	v_mfma_f32_16x16x32_bf16 v[106:109], v[154:157], v[162:165], v[106:109]
	v_mfma_f32_16x16x32_bf16 v[94:97], v[146:149], v[170:173], v[94:97]
	v_mfma_f32_16x16x32_bf16 v[90:93], v[154:157], v[170:173], v[90:93]
	v_mfma_f32_16x16x32_bf16 v[78:81], v[146:149], v[178:181], v[78:81]
	v_mfma_f32_16x16x32_bf16 v[74:77], v[154:157], v[178:181], v[74:77]
	v_mfma_f32_16x16x32_bf16 v[70:73], v[146:149], v[186:189], v[70:73]
	v_mfma_f32_16x16x32_bf16 v[66:69], v[154:157], v[186:189], v[66:69]
	v_mfma_f32_16x16x32_bf16 v[110:113], v[150:153], v[166:169], v[110:113]
	v_mfma_f32_16x16x32_bf16 v[106:109], v[158:161], v[166:169], v[106:109]
	v_mfma_f32_16x16x32_bf16 v[94:97], v[150:153], v[174:177], v[94:97]
	v_mfma_f32_16x16x32_bf16 v[90:93], v[158:161], v[174:177], v[90:93]
	v_mfma_f32_16x16x32_bf16 v[78:81], v[150:153], v[182:185], v[78:81]
	v_mfma_f32_16x16x32_bf16 v[74:77], v[158:161], v[182:185], v[74:77]
	v_mfma_f32_16x16x32_bf16 v[70:73], v[150:153], v[190:193], v[70:73]
	v_mfma_f32_16x16x32_bf16 v[66:69], v[158:161], v[190:193], v[66:69]
	s_setprio 0
	s_barrier
; #define G8_STAGE(bufoff, gbase, voff) do { _Pragma("unroll") for (int _i = 0; _i < 2; ++_i) \
;         __builtin_amdgcn_global_load_lds((const unsigned*)((const char*)(gbase) + (voff)[_i]), (LAS unsigned*)(lds + (bufoff) + ldsw + _i * 8192), 16, 0, 0); } while (0)
; #define G8_LDA(dst, b, h) do { _Pragma("unroll") for (int m = 0; m < 4; ++m) _Pragma("unroll") for (int k = 0; k < 2; ++k) dst[m][k] = *(const LAS bf16x8*)(lds + G8_SA(b, h) + aoff + m * 2048 + k * 1024); } while (0)
; #define G8_WAIT_V(n) asm volatile("s_waitcnt vmcnt(" #n ")" ::: "memory")
; #define G8_WAIT_L(n) asm volatile("s_waitcnt lgkmcnt(" #n ")" ::: "memory")
; #define G8_BAR __builtin_amdgcn_s_barrier()
; #define G8_SCHED __builtin_amdgcn_sched_barrier(0)
; template <class Epi, class Sched, int NT, bool F8 = false>
; __device__ __forceinline__ void gemm_phase(LAS unsigned char* lds, const Sched& S, const Epi& E) {
;     ...
;             G8_LDA(At, 1, 1); G8_STAGE(G8_SB(1, 0), b3, voffB); G8_STAGE(G8_SB(1, 1), b3, voffB1); G8_STAGE(G8_SA(1, 0), a3, cur.vA0);
;             G8_WAIT_V(8); G8_WAIT_L(0); G8_BAR; G8_MMA(1, 0, At, B0); G8_MMA(1, 1, At, B1); G8_BAR; G8_SCHED;
;         }
	s_add_i32 s24, s46, s31
	v_lshl_add_u64 v[226:227], v[240:241], 0, s[8:9]
	s_mov_b32 m0, s24
	ds_read_b128 v[162:165], v236 offset:49152
	ds_read_b128 v[166:169], v236 offset:50176
	ds_read_b128 v[170:173], v236 offset:51200
	ds_read_b128 v[174:177], v236 offset:52224
	ds_read_b128 v[178:181], v236 offset:53248
	ds_read_b128 v[182:185], v236 offset:54272
	ds_read_b128 v[186:189], v236 offset:55296
	ds_read_b128 v[190:193], v236 offset:56320
	global_load_lds_dwordx4 v[226:227], off
	v_lshl_add_u64 v[226:227], v[242:243], 0, s[8:9]
	s_add_i32 m0, s24, 0x2000
	s_add_i32 s24, s47, s31
	global_load_lds_dwordx4 v[226:227], off
	v_lshl_add_u64 v[226:227], s[22:23], 0, v[200:201]
	s_mov_b32 m0, s24
	s_nop 0
	global_load_lds_dwordx4 v[226:227], off
	v_lshl_add_u64 v[226:227], s[22:23], 0, v[204:205]
	s_add_i32 m0, s24, 0x2000
	s_nop 0
	global_load_lds_dwordx4 v[226:227], off
	v_lshl_add_u64 v[226:227], v[244:245], 0, s[8:9]
	s_mov_b32 m0, s43
	s_nop 0
	global_load_lds_dwordx4 v[226:227], off
	v_lshl_add_u64 v[226:227], v[246:247], 0, s[8:9]
	s_mov_b32 m0, s44
	s_nop 0
	global_load_lds_dwordx4 v[226:227], off
	s_waitcnt vmcnt(8)
	s_waitcnt lgkmcnt(0)
	s_barrier
	s_setprio 1
	s_waitcnt lgkmcnt(0)
	v_mfma_f32_16x16x32_bf16 v[62:65], v[130:133], v[162:165], v[62:65]
	v_mfma_f32_16x16x32_bf16 v[58:61], v[138:141], v[162:165], v[58:61]
	v_mfma_f32_16x16x32_bf16 v[54:57], v[130:133], v[170:173], v[54:57]
	v_mfma_f32_16x16x32_bf16 v[50:53], v[138:141], v[170:173], v[50:53]
	v_mfma_f32_16x16x32_bf16 v[38:41], v[130:133], v[178:181], v[38:41]
	v_mfma_f32_16x16x32_bf16 v[34:37], v[138:141], v[178:181], v[34:37]
	v_mfma_f32_16x16x32_bf16 v[22:25], v[130:133], v[186:189], v[22:25]
	v_mfma_f32_16x16x32_bf16 v[18:21], v[138:141], v[186:189], v[18:21]
	v_mfma_f32_16x16x32_bf16 v[62:65], v[134:137], v[166:169], v[62:65]
	v_mfma_f32_16x16x32_bf16 v[58:61], v[142:145], v[166:169], v[58:61]
	v_mfma_f32_16x16x32_bf16 v[54:57], v[134:137], v[174:177], v[54:57]
	v_mfma_f32_16x16x32_bf16 v[50:53], v[142:145], v[174:177], v[50:53]
	v_mfma_f32_16x16x32_bf16 v[38:41], v[134:137], v[182:185], v[38:41]
	v_mfma_f32_16x16x32_bf16 v[34:37], v[142:145], v[182:185], v[34:37]
	v_mfma_f32_16x16x32_bf16 v[22:25], v[134:137], v[190:193], v[22:25]
	v_mfma_f32_16x16x32_bf16 v[18:21], v[142:145], v[190:193], v[18:21]
	s_setprio 0
	s_setprio 1
	v_mfma_f32_16x16x32_bf16 v[46:49], v[146:149], v[162:165], v[46:49]
	v_mfma_f32_16x16x32_bf16 v[42:45], v[154:157], v[162:165], v[42:45]
	v_mfma_f32_16x16x32_bf16 v[30:33], v[146:149], v[170:173], v[30:33]
	v_mfma_f32_16x16x32_bf16 v[26:29], v[154:157], v[170:173], v[26:29]
	v_mfma_f32_16x16x32_bf16 v[14:17], v[146:149], v[178:181], v[14:17]
	v_mfma_f32_16x16x32_bf16 v[10:13], v[154:157], v[178:181], v[10:13]
	v_mfma_f32_16x16x32_bf16 v[6:9], v[146:149], v[186:189], v[6:9]
	v_mfma_f32_16x16x32_bf16 v[2:5], v[154:157], v[186:189], v[2:5]
	v_mfma_f32_16x16x32_bf16 v[46:49], v[150:153], v[166:169], v[46:49]
	v_mfma_f32_16x16x32_bf16 v[42:45], v[158:161], v[166:169], v[42:45]
	v_mfma_f32_16x16x32_bf16 v[30:33], v[150:153], v[174:177], v[30:33]
	v_mfma_f32_16x16x32_bf16 v[26:29], v[158:161], v[174:177], v[26:29]
	v_mfma_f32_16x16x32_bf16 v[14:17], v[150:153], v[182:185], v[14:17]
	v_mfma_f32_16x16x32_bf16 v[10:13], v[158:161], v[182:185], v[10:13]
	v_mfma_f32_16x16x32_bf16 v[6:9], v[150:153], v[190:193], v[6:9]
	v_mfma_f32_16x16x32_bf16 v[2:5], v[158:161], v[190:193], v[2:5]
	s_setprio 0
	s_barrier
	s_add_u32 s6, s6, 0x100
	s_addc_u32 s7, s7, 0
	s_add_u32 s26, s26, 0x100
	s_addc_u32 s27, s27, 0
	s_cmp_gt_u32 s53, 29
	s_cbranch_scc1 .LBB0_208
	.p2align 6

; #define LAS __attribute__((address_space(3)))
; __device__ __forceinline__ unsigned pk2(float lo, float hi) { unsigned r; asm volatile("v_cvt_pk_bf16_f32 %0, %1, %2" : "=v"(r) : "v"(lo), "v"(hi)); return r; }
; __device__ __forceinline__ float bflo(unsigned w) { return __uint_as_float(w << 16); }
; __device__ __forceinline__ float bfhi(unsigned w) { return __uint_as_float(w & 0xffff0000u); }
; template <int NET> __device__ __forceinline__ void ret_item(Ctx& F, int item) {
;     ...
;         for (int rr = 0; rr < 4; ++rr) dcm[mt][rr] = __builtin_amdgcn_exp2f(lg2 * (float)((16 * w + fr) - (16 * mt + 4 * fq + rr)));
; #pragma unroll
;     for (int et = 0; et < NET; ++et) st[et] = (f32x4){0.f, 0.f, 0.f, 0.f};
;     __syncthreads();
;     for (int i = tid; i < EW * LP; i += NWAVES * 64) STL[i] = 0;
;     auto ret_stage = [&]() __attribute__((always_inline)) {
; #pragma unroll
;             for (int hh = 0; hh < 2; ++hh) { unsigned oq1[4], oq2[4], ok1[4], ok2[4];
; #pragma unroll
;                 for (int c = 0; c < 4; ++c) { float a[2], bq[2], ka[2], kb[2];
; #pragma unroll
;                     for (int z = 0; z < 2; ++z) { const int jj = hh * 8 + c * 2 + z; const unsigned cw_ = cs4[jj >> 2][jj & 3]; const f32x2 sc = (f32x2){bflo(cw_), bfhi(cw_)};
;                         const float x1 = z ? bfhi(q1[hh][c]) : bflo(q1[hh][c]), x2 = z ? bfhi(q2[hh][c]) : bflo(q2[hh][c]);
;                         const float y1 = z ? bfhi(k1[hh][c]) : bflo(k1[hh][c]), y2 = z ? bfhi(k2[hh][c]) : bflo(k2[hh][c]);
;                         a[z] = (x1 * sc.x - x2 * sc.y) * 0.08838834764831845f; bq[z] = (x2 * sc.x + x1 * sc.y) * 0.08838834764831845f;
;                         ka[z] = y1 * sc.x - y2 * sc.y; kb[z] = y2 * sc.x + y1 * sc.y;
;                     }
;                     oq1[c] = pk2(a[0], a[1]); oq2[c] = pk2(bq[0], bq[1]); ok1[c] = pk2(ka[0], ka[1]); ok2[c] = pk2(kb[0], kb[1]); }
;                 *(LAS u32x4*)(qL + r * LP + j0 + hh * 8) = (u32x4){oq1[0], oq1[1], oq1[2], oq1[3]}; *(LAS u32x4*)(qL + r * LP + 64 + j0 + hh * 8) = (u32x4){oq2[0], oq2[1], oq2[2], oq2[3]};
;                 *(LAS u32x4*)(kL + r * LP + j0 + hh * 8) = (u32x4){ok1[0], ok1[1], ok1[2], ok1[3]}; *(LAS u32x4*)(kL + r * LP + 64 + j0 + hh * 8) = (u32x4){ok2[0], ok2[1], ok2[2], ok2[3]}; }
.LBB0_312:
	v_add_u32_e32 v61, 0x200, v61
	s_movk_i32 s0, 0x1fff
	v_cmp_lt_u32_e64 s[0:1], s0, v61
	ds_write_b16 v60, v107
	s_or_b64 s[84:85], s[0:1], s[84:85]
	v_add_u32_e32 v60, 0x400, v60
	s_andn2_b64 exec, exec, s[84:85]
	s_cbranch_execnz .LBB0_312
	s_or_b64 exec, exec, s[84:85]
	v_mul_f32_e32 v60, v58, v129
	v_mul_f32_e32 v61, v58, v228
	v_mul_f32_e32 v64, v58, v252
	v_mul_f32_e32 v65, v58, v134
	v_mul_f32_e32 v66, v58, v135
	v_mul_f32_e32 v67, v58, v136
	v_exp_f32_e32 v196, v60
	v_exp_f32_e32 v197, v61
	v_exp_f32_e32 v200, v64
	v_exp_f32_e32 v201, v65
	v_and_b32_e32 v60, 0xffff0000, v54
	v_lshlrev_b32_e32 v61, 16, v54
	v_lshlrev_b32_e32 v65, 16, v38
	v_lshlrev_b32_e32 v64, 16, v34
	v_mul_f32_e32 v59, 0x43000000, v59
	v_exp_f32_e32 v202, v66
	v_exp_f32_e32 v203, v67
	v_pk_mul_f32 v[66:67], v[60:61], v[64:65] op_sel:[1,0] op_sel_hi:[0,1]
	v_mul_f32_e32 v59, 0x3fb8aa3b, v59
	v_mul_f32_e32 v62, v58, v229
	v_mul_f32_e32 v63, v58, v231
	v_sub_f32_e32 v54, v66, v67
	v_pk_mul_f32 v[64:65], v[64:65], v[60:61]
	v_exp_f32_e32 v114, v59
	v_exp_f32_e32 v198, v62
	v_exp_f32_e32 v199, v63
	v_lshlrev_b32_e32 v63, 16, v46
	v_lshlrev_b32_e32 v62, 16, v42
	v_mul_f32_e32 v59, 0x3db504f3, v54
	v_add_f32_e32 v54, v64, v65
	v_mul_f32_e32 v68, v58, v137
	v_mul_f32_e32 v66, 0x3db504f3, v54
	v_pk_mul_f32 v[64:65], v[60:61], v[62:63] op_sel:[1,0] op_sel_hi:[0,1]
	v_pk_mul_f32 v[60:61], v[62:63], v[60:61]
	v_and_b32_e32 v54, 0xffff0000, v55
	v_lshlrev_b32_e32 v55, 16, v55
	v_and_b32_e32 v63, 0xffff0000, v38
	v_and_b32_e32 v62, 0xffff0000, v34
	v_exp_f32_e32 v204, v68
	v_sub_f32_e32 v67, v64, v65
	v_add_f32_e32 v68, v60, v61
	v_and_b32_e32 v61, 0xffff0000, v46
	v_and_b32_e32 v60, 0xffff0000, v42
	v_pk_mul_f32 v[64:65], v[54:55], v[62:63] op_sel:[1,0] op_sel_hi:[0,1]
	v_pk_mul_f32 v[62:63], v[62:63], v[54:55]
	v_sub_f32_e32 v34, v64, v65
	v_add_f32_e32 v38, v62, v63
	v_pk_mul_f32 v[62:63], v[54:55], v[60:61] op_sel:[1,0] op_sel_hi:[0,1]
	v_pk_mul_f32 v[54:55], v[60:61], v[54:55]
	v_sub_f32_e32 v42, v62, v63
	v_add_f32_e32 v46, v54, v55
	v_and_b32_e32 v54, 0xffff0000, v56
	v_lshlrev_b32_e32 v55, 16, v56
	v_lshlrev_b32_e32 v63, 16, v39
	v_lshlrev_b32_e32 v62, 16, v35
	v_pk_mul_f32 v[64:65], v[54:55], v[62:63] op_sel:[1,0] op_sel_hi:[0,1]
	v_mul_f32_e32 v34, 0x3db504f3, v34
	v_lshlrev_b32_e32 v61, 16, v47
	v_lshlrev_b32_e32 v60, 16, v43
	v_sub_f32_e32 v56, v64, v65
	v_pk_mul_f32 v[62:63], v[62:63], v[54:55]
	s_waitcnt lgkmcnt(0)
	s_barrier
	v_mul_f32_e32 v38, 0x3db504f3, v38
	v_cvt_pk_bf16_f32 v34, v59, v34
	v_mul_f32_e32 v59, 0x3db504f3, v56
	v_add_f32_e32 v56, v62, v63
	v_pk_mul_f32 v[62:63], v[54:55], v[60:61] op_sel:[1,0] op_sel_hi:[0,1]
	v_pk_mul_f32 v[54:55], v[60:61], v[54:55]
	v_cvt_pk_bf16_f32 v38, v66, v38
	v_and_b32_e32 v61, 0xffff0000, v39
	v_add_f32_e32 v66, v54, v55
	v_and_b32_e32 v54, 0xffff0000, v57
	v_lshlrev_b32_e32 v55, 16, v57
	v_and_b32_e32 v60, 0xffff0000, v35
	v_mul_f32_e32 v64, 0x3db504f3, v56
	v_sub_f32_e32 v65, v62, v63
	v_and_b32_e32 v57, 0xffff0000, v47
	v_and_b32_e32 v56, 0xffff0000, v43
	v_pk_mul_f32 v[62:63], v[54:55], v[60:61] op_sel:[1,0] op_sel_hi:[0,1]
	v_pk_mul_f32 v[60:61], v[60:61], v[54:55]
	v_sub_f32_e32 v35, v62, v63
	v_add_f32_e32 v39, v60, v61
	v_pk_mul_f32 v[60:61], v[54:55], v[56:57] op_sel:[1,0] op_sel_hi:[0,1]
	v_pk_mul_f32 v[54:55], v[56:57], v[54:55]
	v_sub_f32_e32 v43, v60, v61
	v_add_f32_e32 v47, v54, v55
	v_and_b32_e32 v54, 0xffff0000, v50
	v_lshlrev_b32_e32 v55, 16, v50
	v_lshlrev_b32_e32 v61, 16, v40
	v_lshlrev_b32_e32 v60, 16, v36
	v_pk_mul_f32 v[62:63], v[54:55], v[60:61] op_sel:[1,0] op_sel_hi:[0,1]
	v_mul_f32_e32 v35, 0x3db504f3, v35
	v_sub_f32_e32 v50, v62, v63
	v_pk_mul_f32 v[60:61], v[60:61], v[54:55]
	v_cvt_pk_bf16_f32 v42, v67, v42
	v_cvt_pk_bf16_f32 v46, v68, v46
	v_cvt_pk_bf16_f32 v35, v59, v35
	v_lshlrev_b32_e32 v57, 16, v48
	v_lshlrev_b32_e32 v56, 16, v44
	v_mul_f32_e32 v59, 0x3db504f3, v50
	v_add_f32_e32 v50, v60, v61
	v_mul_f32_e32 v39, 0x3db504f3, v39
	v_mul_f32_e32 v62, 0x3db504f3, v50
	v_pk_mul_f32 v[60:61], v[54:55], v[56:57] op_sel:[1,0] op_sel_hi:[0,1]
	v_pk_mul_f32 v[54:55], v[56:57], v[54:55]
	v_and_b32_e32 v50, 0xffff0000, v51
	v_lshlrev_b32_e32 v51, 16, v51
	v_and_b32_e32 v57, 0xffff0000, v40
	v_and_b32_e32 v56, 0xffff0000, v36
	v_cvt_pk_bf16_f32 v39, v64, v39
	v_sub_f32_e32 v63, v60, v61
	v_add_f32_e32 v64, v54, v55
	v_and_b32_e32 v55, 0xffff0000, v48
	v_and_b32_e32 v54, 0xffff0000, v44
	v_pk_mul_f32 v[60:61], v[50:51], v[56:57] op_sel:[1,0] op_sel_hi:[0,1]
	v_pk_mul_f32 v[56:57], v[56:57], v[50:51]
	v_sub_f32_e32 v36, v60, v61
	v_add_f32_e32 v40, v56, v57
	v_pk_mul_f32 v[56:57], v[50:51], v[54:55] op_sel:[1,0] op_sel_hi:[0,1]
	v_pk_mul_f32 v[50:51], v[54:55], v[50:51]
	v_sub_f32_e32 v44, v56, v57
	v_add_f32_e32 v48, v50, v51
	v_and_b32_e32 v50, 0xffff0000, v52
	v_lshlrev_b32_e32 v51, 16, v52
	v_lshlrev_b32_e32 v57, 16, v41
	v_lshlrev_b32_e32 v56, 16, v37
	v_pk_mul_f32 v[60:61], v[50:51], v[56:57] op_sel:[1,0] op_sel_hi:[0,1]
	v_mul_f32_e32 v36, 0x3db504f3, v36
	v_lshlrev_b32_e32 v55, 16, v49
	v_lshlrev_b32_e32 v54, 16, v45
	v_sub_f32_e32 v52, v60, v61
	v_pk_mul_f32 v[56:57], v[56:57], v[50:51]
	v_cvt_pk_bf16_f32 v43, v65, v43
	v_cvt_pk_bf16_f32 v47, v66, v47
	v_mul_f32_e32 v40, 0x3db504f3, v40
	v_cvt_pk_bf16_f32 v36, v59, v36
	v_mul_f32_e32 v59, 0x3db504f3, v52
	v_add_f32_e32 v52, v56, v57
	v_pk_mul_f32 v[56:57], v[50:51], v[54:55] op_sel:[1,0] op_sel_hi:[0,1]
	v_pk_mul_f32 v[50:51], v[54:55], v[50:51]
	v_cvt_pk_bf16_f32 v40, v62, v40
	v_and_b32_e32 v55, 0xffff0000, v41
	v_add_f32_e32 v62, v50, v51
	v_and_b32_e32 v50, 0xffff0000, v53
	v_lshlrev_b32_e32 v51, 16, v53
; #define LAS __attribute__((address_space(3)))
; __device__ __forceinline__ unsigned pk2(float lo, float hi) { unsigned r; asm volatile("v_cvt_pk_bf16_f32 %0, %1, %2" : "=v"(r) : "v"(lo), "v"(hi)); return r; }
; __device__ __forceinline__ float bflo(unsigned w) { return __uint_as_float(w << 16); }
; __device__ __forceinline__ float bfhi(unsigned w) { return __uint_as_float(w & 0xffff0000u); }
; template <int NET> __device__ __forceinline__ void ret_item(Ctx& F, int item) {
;     ...
;             for (int hh = 0; hh < 2; ++hh) { unsigned oq1[4], oq2[4], ok1[4], ok2[4];
; #pragma unroll
;                 for (int c = 0; c < 4; ++c) { float a[2], bq[2], ka[2], kb[2];
; #pragma unroll
;                     for (int z = 0; z < 2; ++z) { const int jj = hh * 8 + c * 2 + z; const unsigned cw_ = cs4[jj >> 2][jj & 3]; const f32x2 sc = (f32x2){bflo(cw_), bfhi(cw_)};
;                         const float x1 = z ? bfhi(q1[hh][c]) : bflo(q1[hh][c]), x2 = z ? bfhi(q2[hh][c]) : bflo(q2[hh][c]);
;                         const float y1 = z ? bfhi(k1[hh][c]) : bflo(k1[hh][c]), y2 = z ? bfhi(k2[hh][c]) : bflo(k2[hh][c]);
;                         a[z] = (x1 * sc.x - x2 * sc.y) * 0.08838834764831845f; bq[z] = (x2 * sc.x + x1 * sc.y) * 0.08838834764831845f;
;                         ka[z] = y1 * sc.x - y2 * sc.y; kb[z] = y2 * sc.x + y1 * sc.y;
;                     }
;                     oq1[c] = pk2(a[0], a[1]); oq2[c] = pk2(bq[0], bq[1]); ok1[c] = pk2(ka[0], ka[1]); ok2[c] = pk2(kb[0], kb[1]); }
;                 *(LAS u32x4*)(qL + r * LP + j0 + hh * 8) = (u32x4){oq1[0], oq1[1], oq1[2], oq1[3]}; *(LAS u32x4*)(qL + r * LP + 64 + j0 + hh * 8) = (u32x4){oq2[0], oq2[1], oq2[2], oq2[3]};
;                 *(LAS u32x4*)(kL + r * LP + j0 + hh * 8) = (u32x4){ok1[0], ok1[1], ok1[2], ok1[3]}; *(LAS u32x4*)(kL + r * LP + 64 + j0 + hh * 8) = (u32x4){ok2[0], ok2[1], ok2[2], ok2[3]}; }
	v_and_b32_e32 v54, 0xffff0000, v37
	v_sub_f32_e32 v61, v56, v57
	v_pk_mul_f32 v[56:57], v[50:51], v[54:55] op_sel:[1,0] op_sel_hi:[0,1]
	v_mul_f32_e32 v60, 0x3db504f3, v52
	v_and_b32_e32 v53, 0xffff0000, v49
	v_and_b32_e32 v52, 0xffff0000, v45
	v_sub_f32_e32 v37, v56, v57
	v_pk_mul_f32 v[54:55], v[54:55], v[50:51]
	v_mul_f32_e32 v37, 0x3db504f3, v37
	v_add_f32_e32 v41, v54, v55
	v_pk_mul_f32 v[54:55], v[50:51], v[52:53] op_sel:[1,0] op_sel_hi:[0,1]
	v_pk_mul_f32 v[50:51], v[52:53], v[50:51]
	v_cvt_pk_bf16_f32 v44, v63, v44
	v_cvt_pk_bf16_f32 v48, v64, v48
	v_mul_f32_e32 v41, 0x3db504f3, v41
	v_sub_f32_e32 v45, v54, v55
	v_add_f32_e32 v49, v50, v51
	v_cvt_pk_bf16_f32 v37, v59, v37
	v_cvt_pk_bf16_f32 v41, v60, v41
	v_cvt_pk_bf16_f32 v45, v61, v45
	v_cvt_pk_bf16_f32 v49, v62, v49
	ds_write_b128 v161, v[34:37]
	ds_write_b128 v161, v[38:41] offset:128
	ds_write_b128 v161, v[42:45] offset:34816
	ds_write_b128 v161, v[46:49] offset:34944
	v_lshlrev_b32_e32 v34, 16, v30
	v_and_b32_e32 v35, 0xffff0000, v30
	v_lshlrev_b32_e32 v37, 16, v14
	v_lshlrev_b32_e32 v36, 16, v10
	v_pk_mul_f32 v[38:39], v[36:37], v[34:35]
	v_pk_mul_f32 v[36:37], v[34:35], v[36:37] op_sel:[1,0] op_sel_hi:[0,1]
	v_sub_f32_e32 v30, v38, v39
	v_mul_f32_e32 v40, 0x3db504f3, v30
	v_add_f32_e32 v30, v36, v37
	v_lshlrev_b32_e32 v37, 16, v22
	v_lshlrev_b32_e32 v36, 16, v18
	v_pk_mul_f32 v[38:39], v[36:37], v[34:35]
	v_pk_mul_f32 v[34:35], v[34:35], v[36:37] op_sel:[1,0] op_sel_hi:[0,1]
	v_mul_f32_e32 v41, 0x3db504f3, v30
	v_sub_f32_e32 v38, v38, v39
	v_add_f32_e32 v39, v34, v35
	v_lshlrev_b32_e32 v30, 16, v31
	v_and_b32_e32 v31, 0xffff0000, v31
	v_and_b32_e32 v35, 0xffff0000, v14
	v_and_b32_e32 v34, 0xffff0000, v10
	v_pk_mul_f32 v[36:37], v[34:35], v[30:31]
	v_pk_mul_f32 v[34:35], v[30:31], v[34:35] op_sel:[1,0] op_sel_hi:[0,1]
	v_add_f32_e32 v14, v34, v35
	v_and_b32_e32 v35, 0xffff0000, v22
	v_and_b32_e32 v34, 0xffff0000, v18
	v_sub_f32_e32 v10, v36, v37
	v_pk_mul_f32 v[36:37], v[34:35], v[30:31]
	v_pk_mul_f32 v[30:31], v[30:31], v[34:35] op_sel:[1,0] op_sel_hi:[0,1]
	v_add_f32_e32 v22, v30, v31
	v_lshlrev_b32_e32 v30, 16, v32
	v_and_b32_e32 v31, 0xffff0000, v32
	v_lshlrev_b32_e32 v35, 16, v15
	v_lshlrev_b32_e32 v34, 16, v11
	v_sub_f32_e32 v18, v36, v37
	v_pk_mul_f32 v[36:37], v[34:35], v[30:31]
	v_mul_f32_e32 v10, 0x3db504f3, v10
	v_mul_f32_e32 v14, 0x3db504f3, v14
	v_sub_f32_e32 v32, v36, v37
	v_pk_mul_f32 v[34:35], v[30:31], v[34:35] op_sel:[1,0] op_sel_hi:[0,1]
	v_cvt_pk_bf16_f32 v10, v40, v10
	v_cvt_pk_bf16_f32 v14, v41, v14
	v_cvt_pk_bf16_f32 v18, v38, v18
	v_mul_f32_e32 v38, 0x3db504f3, v32
	v_add_f32_e32 v32, v34, v35
	v_lshlrev_b32_e32 v35, 16, v23
	v_lshlrev_b32_e32 v34, 16, v19
	v_pk_mul_f32 v[36:37], v[34:35], v[30:31]
	v_pk_mul_f32 v[30:31], v[30:31], v[34:35] op_sel:[1,0] op_sel_hi:[0,1]
	v_cvt_pk_bf16_f32 v22, v39, v22
	v_mul_f32_e32 v39, 0x3db504f3, v32
	v_sub_f32_e32 v36, v36, v37
	v_add_f32_e32 v37, v30, v31
	v_lshlrev_b32_e32 v30, 16, v33
	v_and_b32_e32 v31, 0xffff0000, v33
	v_and_b32_e32 v33, 0xffff0000, v15
	v_and_b32_e32 v32, 0xffff0000, v11
	v_pk_mul_f32 v[34:35], v[32:33], v[30:31]
	v_pk_mul_f32 v[32:33], v[30:31], v[32:33] op_sel:[1,0] op_sel_hi:[0,1]
	v_add_f32_e32 v15, v32, v33
	v_and_b32_e32 v33, 0xffff0000, v23
	v_and_b32_e32 v32, 0xffff0000, v19
	v_sub_f32_e32 v11, v34, v35
	v_pk_mul_f32 v[34:35], v[32:33], v[30:31]
	v_pk_mul_f32 v[30:31], v[30:31], v[32:33] op_sel:[1,0] op_sel_hi:[0,1]
	v_add_f32_e32 v23, v30, v31
	v_lshlrev_b32_e32 v30, 16, v26
	v_and_b32_e32 v31, 0xffff0000, v26
	v_lshlrev_b32_e32 v33, 16, v16
	v_lshlrev_b32_e32 v32, 16, v12
	v_sub_f32_e32 v19, v34, v35
	v_pk_mul_f32 v[34:35], v[32:33], v[30:31]
	v_mul_f32_e32 v11, 0x3db504f3, v11
	v_mul_f32_e32 v15, 0x3db504f3, v15
	v_sub_f32_e32 v26, v34, v35
	v_pk_mul_f32 v[32:33], v[30:31], v[32:33] op_sel:[1,0] op_sel_hi:[0,1]
	v_cvt_pk_bf16_f32 v11, v38, v11
	v_cvt_pk_bf16_f32 v15, v39, v15
	v_cvt_pk_bf16_f32 v19, v36, v19
	v_mul_f32_e32 v36, 0x3db504f3, v26
	v_add_f32_e32 v26, v32, v33
	v_lshlrev_b32_e32 v33, 16, v24
	v_lshlrev_b32_e32 v32, 16, v20
	v_pk_mul_f32 v[34:35], v[32:33], v[30:31]
	v_pk_mul_f32 v[30:31], v[30:31], v[32:33] op_sel:[1,0] op_sel_hi:[0,1]
	v_cvt_pk_bf16_f32 v23, v37, v23
	v_mul_f32_e32 v37, 0x3db504f3, v26
	v_sub_f32_e32 v34, v34, v35
	v_add_f32_e32 v35, v30, v31
	v_lshlrev_b32_e32 v26, 16, v27
	v_and_b32_e32 v27, 0xffff0000, v27
	v_and_b32_e32 v31, 0xffff0000, v16
	v_and_b32_e32 v30, 0xffff0000, v12
	v_pk_mul_f32 v[32:33], v[30:31], v[26:27]
	v_pk_mul_f32 v[30:31], v[26:27], v[30:31] op_sel:[1,0] op_sel_hi:[0,1]
	v_add_f32_e32 v16, v30, v31
	v_and_b32_e32 v31, 0xffff0000, v24
	v_and_b32_e32 v30, 0xffff0000, v20
	v_sub_f32_e32 v12, v32, v33
	v_pk_mul_f32 v[32:33], v[30:31], v[26:27]
	v_pk_mul_f32 v[26:27], v[26:27], v[30:31] op_sel:[1,0] op_sel_hi:[0,1]
	v_add_f32_e32 v24, v26, v27
	v_and_b32_e32 v26, 0xffff0000, v28
	v_lshlrev_b32_e32 v27, 16, v28
	v_lshlrev_b32_e32 v31, 16, v25
	v_lshlrev_b32_e32 v30, 16, v21
	v_mul_f32_e32 v12, 0x3db504f3, v12
	v_mul_f32_e32 v16, 0x3db504f3, v16
	v_sub_f32_e32 v20, v32, v33
; template <int NET> __device__ __forceinline__ void ret_item(Ctx& F, int item) {
;     ...
;         for (int rr = 0; rr < 4; ++rr) dcm[mt][rr] = __builtin_amdgcn_exp2f(lg2 * (float)((16 * w + fr) - (16 * mt + 4 * fq + rr)));
; #pragma unroll
;     for (int et = 0; et < NET; ++et) st[et] = (f32x4){0.f, 0.f, 0.f, 0.f};
;     __syncthreads();
;     for (int i = tid; i < EW * LP; i += NWAVES * 64) STL[i] = 0;
;     auto ret_stage = [&]() __attribute__((always_inline)) {
; #pragma unroll
;             for (int hh = 0; hh < 2; ++hh) { unsigned oq1[4], oq2[4], ok1[4], ok2[4];
; #pragma unroll
;                 for (int c = 0; c < 4; ++c) { float a[2], bq[2], ka[2], kb[2];
; #pragma unroll
;                     for (int z = 0; z < 2; ++z) { const int jj = hh * 8 + c * 2 + z; const unsigned cw_ = cs4[jj >> 2][jj & 3]; const f32x2 sc = (f32x2){bflo(cw_), bfhi(cw_)};
;                         const float x1 = z ? bfhi(q1[hh][c]) : bflo(q1[hh][c]), x2 = z ? bfhi(q2[hh][c]) : bflo(q2[hh][c]);
;                         const float y1 = z ? bfhi(k1[hh][c]) : bflo(k1[hh][c]), y2 = z ? bfhi(k2[hh][c]) : bflo(k2[hh][c]);
;                         a[z] = (x1 * sc.x - x2 * sc.y) * 0.08838834764831845f; bq[z] = (x2 * sc.x + x1 * sc.y) * 0.08838834764831845f;
;                         ka[z] = y1 * sc.x - y2 * sc.y; kb[z] = y2 * sc.x + y1 * sc.y;
;                     }
;                     oq1[c] = pk2(a[0], a[1]); oq2[c] = pk2(bq[0], bq[1]); ok1[c] = pk2(ka[0], ka[1]); ok2[c] = pk2(kb[0], kb[1]); }
;                 *(LAS u32x4*)(qL + r * LP + j0 + hh * 8) = (u32x4){oq1[0], oq1[1], oq1[2], oq1[3]}; *(LAS u32x4*)(qL + r * LP + 64 + j0 + hh * 8) = (u32x4){oq2[0], oq2[1], oq2[2], oq2[3]};
;                 *(LAS u32x4*)(kL + r * LP + j0 + hh * 8) = (u32x4){ok1[0], ok1[1], ok1[2], ok1[3]}; *(LAS u32x4*)(kL + r * LP + 64 + j0 + hh * 8) = (u32x4){ok2[0], ok2[1], ok2[2], ok2[3]}; }
; #pragma unroll
;             for (int vi = 0; vi < NET / 2; ++vi) { unsigned vd[4];
; #pragma unroll
;                 for (int c = 0; c < 4; ++c) vd[c] = pk2(bflo(vv[vi][c]) * kdec, bfhi(vv[vi][c]) * kdec);
;                 *(LAS u32x4*)(vL + r * VP + qd * (EW / 4) + 8 * vi) = vv[vi]; *(LAS u32x4*)(vdL + r * VP + qd * (EW / 4) + 8 * vi) = (u32x4){vd[0], vd[1], vd[2], vd[3]}; }
;     };
;     LDS_BARRIER();
;     ret_stage();
; #pragma unroll 1
;     for (int n = 0; n < 16; ++n) {
	v_pk_mul_f32 v[32:33], v[30:31], v[26:27]
	v_pk_mul_f32 v[30:31], v[26:27], v[30:31] op_sel:[1,0] op_sel_hi:[0,1]
	v_cvt_pk_bf16_f32 v12, v36, v12
	v_cvt_pk_bf16_f32 v16, v37, v16
	v_cvt_pk_bf16_f32 v20, v34, v20
	v_cvt_pk_bf16_f32 v24, v35, v24
	v_sub_f32_e32 v35, v30, v31
	v_lshlrev_b32_e32 v31, 16, v17
	v_lshlrev_b32_e32 v30, 16, v13
	v_add_f32_e32 v34, v32, v33
	v_pk_mul_f32 v[32:33], v[30:31], v[26:27]
	v_pk_mul_f32 v[26:27], v[26:27], v[30:31] op_sel:[1,0] op_sel_hi:[0,1]
	v_add_f32_e32 v28, v32, v33
	v_mul_f32_e32 v36, 0x3db504f3, v28
	v_and_b32_e32 v28, 0xffff0000, v29
	v_lshlrev_b32_e32 v29, 16, v29
	v_and_b32_e32 v31, 0xffff0000, v17
	v_and_b32_e32 v30, 0xffff0000, v13
	v_mul_f32_e32 v91, v58, v127
	v_sub_f32_e32 v26, v26, v27
	v_pk_mul_f32 v[32:33], v[28:29], v[30:31] op_sel:[1,0] op_sel_hi:[0,1]
	v_exp_f32_e32 v227, v91
	v_mul_f32_e32 v37, 0x3db504f3, v26
	v_and_b32_e32 v27, 0xffff0000, v25
	v_and_b32_e32 v26, 0xffff0000, v21
	v_sub_f32_e32 v13, v32, v33
	v_pk_mul_f32 v[30:31], v[30:31], v[28:29]
	v_mul_f32_e32 v13, 0x3db504f3, v13
	v_add_f32_e32 v17, v30, v31
	v_pk_mul_f32 v[30:31], v[28:29], v[26:27] op_sel:[1,0] op_sel_hi:[0,1]
	v_pk_mul_f32 v[26:27], v[26:27], v[28:29]
	v_mul_f32_e32 v17, 0x3db504f3, v17
	v_sub_f32_e32 v21, v30, v31
	v_add_f32_e32 v25, v26, v27
	v_cvt_pk_bf16_f32 v13, v37, v13
	v_cvt_pk_bf16_f32 v17, v36, v17
	v_cvt_pk_bf16_f32 v21, v35, v21
	v_cvt_pk_bf16_f32 v25, v34, v25
	ds_write_b128 v161, v[10:13] offset:16
	ds_write_b128 v161, v[14:17] offset:144
	ds_write_b128 v161, v[18:21] offset:34832
	ds_write_b128 v161, v[22:25] offset:34960
	v_lshlrev_b32_e32 v10, 16, v6
	v_and_b32_e32 v11, 0xffff0000, v6
	v_mul_f32_e32 v10, v227, v10
	v_mul_f32_e32 v11, v227, v11
	v_cvt_pk_bf16_f32 v10, v10, v11
	v_lshlrev_b32_e32 v11, 16, v7
	v_and_b32_e32 v12, 0xffff0000, v7
	v_mul_f32_e32 v11, v227, v11
	v_mul_f32_e32 v12, v227, v12
	v_cvt_pk_bf16_f32 v11, v11, v12
	v_lshlrev_b32_e32 v12, 16, v8
	v_and_b32_e32 v13, 0xffff0000, v8
	v_mul_f32_e32 v12, v227, v12
	v_mul_f32_e32 v13, v227, v13
	v_cvt_pk_bf16_f32 v12, v12, v13
	v_lshlrev_b32_e32 v13, 16, v9
	v_mul_f32_e32 v13, v227, v13
	v_and_b32_e32 v14, 0xffff0000, v9
	v_mul_f32_e32 v14, v227, v14
	v_cvt_pk_bf16_f32 v13, v13, v14
	ds_write_b128 v194, v[6:9]
	ds_write_b128 v195, v[10:13]
	v_lshlrev_b32_e32 v6, 16, v2
	v_and_b32_e32 v7, 0xffff0000, v2
	v_mul_f32_e32 v6, v227, v6
	v_mul_f32_e32 v7, v227, v7
	v_cvt_pk_bf16_f32 v6, v6, v7
	v_lshlrev_b32_e32 v7, 16, v3
	v_and_b32_e32 v8, 0xffff0000, v3
	v_mul_f32_e32 v7, v227, v7
	v_mul_f32_e32 v8, v227, v8
	v_cvt_pk_bf16_f32 v7, v7, v8
	v_lshlrev_b32_e32 v8, 16, v4
	v_and_b32_e32 v9, 0xffff0000, v4
	v_mul_f32_e32 v8, v227, v8
	v_mul_f32_e32 v9, v227, v9
	v_cvt_pk_bf16_f32 v8, v8, v9
	v_lshlrev_b32_e32 v9, 16, v5
	s_lshl_b32 s0, s94, 1
	v_mul_f32_e32 v9, v227, v9
	v_and_b32_e32 v10, 0xffff0000, v5
	s_add_u32 s88, s76, s0
	v_mul_f32_e32 v10, v227, v10
	v_cvt_pk_bf16_f32 v9, v9, v10
	ds_write_b128 v194, v[2:5] offset:16
	ds_write_b128 v195, v[6:9] offset:16
	s_addc_u32 s89, s77, 0
	v_mul_f32_e32 v2, v58, v165
	s_lshl_b32 s0, s94, 2
	v_mul_f32_e32 v69, v58, v138
	v_mul_f32_e32 v70, v58, v139
	v_mul_f32_e32 v71, v58, v140
	v_mul_f32_e32 v72, v58, v141
	v_mul_f32_e32 v73, v58, v142
	v_mul_f32_e32 v74, v58, v143
	v_mul_f32_e32 v75, v58, v144
	v_mul_f32_e32 v76, v58, v145
	v_mul_f32_e32 v77, v58, v146
	v_mul_f32_e32 v78, v58, v147
	v_mul_f32_e32 v79, v58, v148
	v_mul_f32_e32 v80, v58, v149
	v_mul_f32_e32 v81, v58, v150
	v_mul_f32_e32 v82, v58, v151
	v_mul_f32_e32 v83, v58, v152
	v_mul_f32_e32 v84, v58, v153
	v_mul_f32_e32 v85, v58, v154
	v_mul_f32_e32 v86, v58, v155
	v_mul_f32_e32 v87, v58, v156
	v_mul_f32_e32 v88, v58, v157
	v_mul_f32_e32 v89, v58, v158
	v_mul_f32_e32 v90, v58, v159
	v_exp_f32_e32 v116, v2
	s_add_u32 s74, s87, s0
	v_exp_f32_e32 v205, v69
	v_exp_f32_e32 v206, v70
	v_exp_f32_e32 v207, v71
	v_exp_f32_e32 v208, v72
	v_exp_f32_e32 v209, v73
	v_exp_f32_e32 v210, v74
	v_exp_f32_e32 v211, v75
	v_exp_f32_e32 v212, v76
	v_exp_f32_e32 v213, v77
	v_exp_f32_e32 v214, v78
	v_exp_f32_e32 v215, v79
	v_exp_f32_e32 v216, v80
	v_exp_f32_e32 v217, v81
	v_exp_f32_e32 v218, v82
	v_exp_f32_e32 v219, v83
	v_exp_f32_e32 v220, v84
	v_exp_f32_e32 v221, v85
	v_exp_f32_e32 v222, v86
	v_exp_f32_e32 v223, v87
	v_exp_f32_e32 v224, v88
	v_exp_f32_e32 v225, v89
	v_exp_f32_e32 v226, v90
	s_addc_u32 s84, s90, 0
	s_lshl_b64 s[0:1], s[80:81], 2
	s_add_u32 s0, s74, s0
	s_addc_u32 s1, s84, s1
	v_mov_b32_e32 v111, v107
	v_mov_b32_e32 v10, 0
	v_mov_b32_e32 v117, v116
	v_mov_b32_e32 v118, v116
	v_mov_b32_e32 v119, v116
	v_lshl_add_u64 v[120:121], s[0:1], 0, v[110:111]
	v_mov_b32_e32 v122, v114
	v_mov_b32_e32 v123, v114
	v_add_u32_e32 v111, s33, v128
	s_mov_b32 s33, 0
	v_mov_b32_e32 v11, v10
	v_mov_b32_e32 v12, v10
	v_mov_b32_e32 v13, v10
	v_mov_b32_e32 v14, v10
	v_mov_b32_e32 v15, v10
	v_mov_b32_e32 v16, v10
	v_mov_b32_e32 v17, v10
	v_mov_b32_e32 v6, v10
	v_mov_b32_e32 v7, v10
	v_mov_b32_e32 v8, v10
	v_mov_b32_e32 v9, v10
	v_mov_b32_e32 v2, v10
	v_mov_b32_e32 v3, v10
	v_mov_b32_e32 v4, v10
	v_mov_b32_e32 v5, v10
	.p2align 6

; #define G8_STAGE(bufoff, gbase, voff) do { _Pragma("unroll") for (int _i = 0; _i < 2; ++_i) \
;         __builtin_amdgcn_global_load_lds((const unsigned*)((const char*)(gbase) + (voff)[_i]), (LAS unsigned*)(lds + (bufoff) + ldsw + _i * 8192), 16, 0, 0); } while (0)
; #define G8_LDA(dst, b, h) do { _Pragma("unroll") for (int m = 0; m < 4; ++m) _Pragma("unroll") for (int k = 0; k < 2; ++k) dst[m][k] = *(const LAS bf16x8*)(lds + G8_SA(b, h) + aoff + m * 2048 + k * 1024); } while (0)
; #define G8_LDB(dst, b, h) do { _Pragma("unroll") for (int n = 0; n < 2; ++n) _Pragma("unroll") for (int k = 0; k < 2; ++k) dst[n][k] = *(const LAS bf16x8*)(lds + G8_SB(b, h) + boff + n * 2048 + k * 1024); } while (0)
; #define G8_WAIT_V(n) asm volatile("s_waitcnt vmcnt(" #n ")" ::: "memory")
; #define G8_WAIT_L(n) asm volatile("s_waitcnt lgkmcnt(" #n ")" ::: "memory")
; #define G8_BAR __builtin_amdgcn_s_barrier()
; #define G8_SCHED __builtin_amdgcn_sched_barrier(0)
; template <class Epi, class Sched, int NT, bool F8 = false>
; __device__ __forceinline__ void gemm_phase(LAS unsigned char* lds, const Sched& S, const Epi& E) {
;     ...
;             G8_WAIT_VF(t, ui); G8_WAIT_L(0); G8_BAR; G8_MMA(1, 0, At, B0); G8_MMA(1, 1, At, B1); G8_BAR; G8_SCHED;
;             G8_LDB(B0, 1, 0); G8_LDB(B1, 1, 1); G8_SCHED; G8_LDA(At, 1, 0); G8_STAGE(G8_SA(0, 1), a2, cur.vA1);
;             G8_WAIT_V(8); G8_WAIT_L(0); G8_BAR; G8_MMA(0, 0, At, B0); G8_MMA(0, 1, At, B1); G8_BAR; G8_SCHED;
;             G8_LDA(At, 1, 1); G8_STAGE(G8_SB(1, 0), b3, voffB); G8_STAGE(G8_SB(1, 1), b3, voffB1); G8_STAGE(G8_SA(1, 0), a3, cur.vA0);
;             G8_WAIT_V(8); G8_WAIT_L(0); G8_BAR; G8_MMA(1, 0, At, B0); G8_MMA(1, 1, At, B1); G8_BAR; G8_SCHED;
;         }
.Lcz_p81r:
	s_setprio 0
	s_barrier
	v_add_u32_e32 v14, s50, v221
	v_add_u32_e32 v30, s51, v221
	ds_read_b128 v[2:5], v14
	ds_read_b128 v[6:9], v14 offset:1024
	ds_read_b128 v[10:13], v14 offset:2048
	ds_read_b128 v[14:17], v14 offset:3072
	ds_read_b128 v[18:21], v30
	ds_read_b128 v[22:25], v30 offset:1024
	ds_read_b128 v[26:29], v30 offset:2048
	ds_read_b128 v[30:33], v30 offset:3072
	s_mov_b32 m0, s45
	v_lshl_add_u64 v[216:217], s[30:31], 0, v[216:217]
	ds_read_b128 v[34:37], v226 offset:32768
	ds_read_b128 v[38:41], v226 offset:33792
	ds_read_b128 v[42:45], v226 offset:34816
	ds_read_b128 v[46:49], v226 offset:35840
	ds_read_b128 v[50:53], v226 offset:36864
	ds_read_b128 v[54:57], v226 offset:37888
	ds_read_b128 v[58:61], v226 offset:38912
	ds_read_b128 v[62:65], v226 offset:39936
	global_load_lds_dwordx4 v[216:217], off
	v_lshl_add_u64 v[214:215], s[30:31], 0, v[214:215]
	s_mov_b32 m0, s47
	s_nop 0
	global_load_lds_dwordx4 v[214:215], off
	s_waitcnt vmcnt(8)
	s_waitcnt lgkmcnt(0)
	s_barrier
	s_setprio 1
	s_waitcnt lgkmcnt(0)
	v_mfma_scale_f32_16x16x128_f8f6f4 v[190:193], v[2:9], v[34:41], v[190:193], v227, v227 op_sel_hi:[0,0,0]
	v_mfma_scale_f32_16x16x128_f8f6f4 v[182:185], v[10:17], v[34:41], v[182:185], v227, v227 op_sel_hi:[0,0,0]
	v_mfma_scale_f32_16x16x128_f8f6f4 v[174:177], v[2:9], v[42:49], v[174:177], v227, v227 op_sel_hi:[0,0,0]
	v_mfma_scale_f32_16x16x128_f8f6f4 v[166:169], v[10:17], v[42:49], v[166:169], v227, v227 op_sel_hi:[0,0,0]
	v_mfma_scale_f32_16x16x128_f8f6f4 v[158:161], v[2:9], v[50:57], v[158:161], v227, v227 op_sel_hi:[0,0,0]
	v_mfma_scale_f32_16x16x128_f8f6f4 v[150:153], v[10:17], v[50:57], v[150:153], v227, v227 op_sel_hi:[0,0,0]
	v_mfma_scale_f32_16x16x128_f8f6f4 v[142:145], v[2:9], v[58:65], v[142:145], v227, v227 op_sel_hi:[0,0,0]
	v_mfma_scale_f32_16x16x128_f8f6f4 v[134:137], v[10:17], v[58:65], v[134:137], v227, v227 op_sel_hi:[0,0,0]
	s_setprio 0
	s_setprio 1
	v_mfma_scale_f32_16x16x128_f8f6f4 v[186:189], v[18:25], v[34:41], v[186:189], v227, v227 op_sel_hi:[0,0,0]
	v_mfma_scale_f32_16x16x128_f8f6f4 v[178:181], v[26:33], v[34:41], v[178:181], v227, v227 op_sel_hi:[0,0,0]
	v_mfma_scale_f32_16x16x128_f8f6f4 v[170:173], v[18:25], v[42:49], v[170:173], v227, v227 op_sel_hi:[0,0,0]
	v_mfma_scale_f32_16x16x128_f8f6f4 v[162:165], v[26:33], v[42:49], v[162:165], v227, v227 op_sel_hi:[0,0,0]
	v_mfma_scale_f32_16x16x128_f8f6f4 v[154:157], v[18:25], v[50:57], v[154:157], v227, v227 op_sel_hi:[0,0,0]
	v_mfma_scale_f32_16x16x128_f8f6f4 v[146:149], v[26:33], v[50:57], v[146:149], v227, v227 op_sel_hi:[0,0,0]
	v_mfma_scale_f32_16x16x128_f8f6f4 v[138:141], v[18:25], v[58:65], v[138:141], v227, v227 op_sel_hi:[0,0,0]
	v_mfma_scale_f32_16x16x128_f8f6f4 v[130:133], v[26:33], v[58:65], v[130:133], v227, v227 op_sel_hi:[0,0,0]
	s_setprio 0
	s_barrier
	s_add_i32 s30, s50, s25
	v_lshl_add_u64 v[214:215], v[232:233], 0, s[2:3]
	s_mov_b32 m0, s30
	ds_read_b128 v[34:37], v226 offset:49152
	ds_read_b128 v[38:41], v226 offset:50176
	ds_read_b128 v[42:45], v226 offset:51200
	ds_read_b128 v[46:49], v226 offset:52224
	ds_read_b128 v[50:53], v226 offset:53248
	ds_read_b128 v[54:57], v226 offset:54272
	ds_read_b128 v[58:61], v226 offset:55296
	ds_read_b128 v[62:65], v226 offset:56320
	global_load_lds_dwordx4 v[214:215], off
	v_lshl_add_u64 v[214:215], v[234:235], 0, s[2:3]
	s_add_i32 m0, s30, 0x2000
	s_add_i32 s30, s51, s25
	global_load_lds_dwordx4 v[214:215], off
	v_lshl_add_u64 v[214:215], s[28:29], 0, v[198:199]
	s_mov_b32 m0, s30
	s_nop 0
	global_load_lds_dwordx4 v[214:215], off
	v_lshl_add_u64 v[214:215], s[28:29], 0, v[202:203]
	s_add_i32 m0, s30, 0x2000
	s_nop 0
	global_load_lds_dwordx4 v[214:215], off
	v_lshl_add_u64 v[214:215], v[236:237], 0, s[2:3]
	s_mov_b32 m0, s48
	s_nop 0
	global_load_lds_dwordx4 v[214:215], off
	v_lshl_add_u64 v[214:215], v[238:239], 0, s[2:3]
	s_mov_b32 m0, s49
	s_nop 0
	global_load_lds_dwordx4 v[214:215], off
	s_waitcnt vmcnt(8)
	s_waitcnt lgkmcnt(0)
	s_barrier
	s_setprio 1
	s_waitcnt lgkmcnt(0)
	v_mfma_scale_f32_16x16x128_f8f6f4 v[126:129], v[2:9], v[34:41], v[126:129], v227, v227 op_sel_hi:[0,0,0]
	v_mfma_scale_f32_16x16x128_f8f6f4 v[118:121], v[10:17], v[34:41], v[118:121], v227, v227 op_sel_hi:[0,0,0]
	v_mfma_scale_f32_16x16x128_f8f6f4 v[110:113], v[2:9], v[42:49], v[110:113], v227, v227 op_sel_hi:[0,0,0]
	v_mfma_scale_f32_16x16x128_f8f6f4 v[102:105], v[10:17], v[42:49], v[102:105], v227, v227 op_sel_hi:[0,0,0]
	v_mfma_scale_f32_16x16x128_f8f6f4 v[94:97], v[2:9], v[50:57], v[94:97], v227, v227 op_sel_hi:[0,0,0]
	v_mfma_scale_f32_16x16x128_f8f6f4 v[86:89], v[10:17], v[50:57], v[86:89], v227, v227 op_sel_hi:[0,0,0]
	v_mfma_scale_f32_16x16x128_f8f6f4 v[78:81], v[2:9], v[58:65], v[78:81], v227, v227 op_sel_hi:[0,0,0]
	v_mfma_scale_f32_16x16x128_f8f6f4 v[70:73], v[10:17], v[58:65], v[70:73], v227, v227 op_sel_hi:[0,0,0]
	s_setprio 0
	s_setprio 1
	v_mfma_scale_f32_16x16x128_f8f6f4 v[122:125], v[18:25], v[34:41], v[122:125], v227, v227 op_sel_hi:[0,0,0]
	v_mfma_scale_f32_16x16x128_f8f6f4 v[114:117], v[26:33], v[34:41], v[114:117], v227, v227 op_sel_hi:[0,0,0]
	v_mfma_scale_f32_16x16x128_f8f6f4 v[106:109], v[18:25], v[42:49], v[106:109], v227, v227 op_sel_hi:[0,0,0]
	v_mfma_scale_f32_16x16x128_f8f6f4 v[98:101], v[26:33], v[42:49], v[98:101], v227, v227 op_sel_hi:[0,0,0]
	v_mfma_scale_f32_16x16x128_f8f6f4 v[90:93], v[18:25], v[50:57], v[90:93], v227, v227 op_sel_hi:[0,0,0]
	v_mfma_scale_f32_16x16x128_f8f6f4 v[82:85], v[26:33], v[50:57], v[82:85], v227, v227 op_sel_hi:[0,0,0]
	v_mfma_scale_f32_16x16x128_f8f6f4 v[74:77], v[18:25], v[58:65], v[74:77], v227, v227 op_sel_hi:[0,0,0]
	v_mfma_scale_f32_16x16x128_f8f6f4 v[66:69], v[26:33], v[58:65], v[66:69], v227, v227 op_sel_hi:[0,0,0]
	s_setprio 0
	s_barrier
	s_add_u32 s26, s26, 0x100
	s_addc_u32 s27, s27, 0
	s_add_u32 s19, s19, 0x100
	s_addc_u32 s57, s57, 0
	s_cmp_gt_u32 s58, 13
	s_cbranch_scc1 .LBB0_846
	.p2align 6

; #define G8_WAIT_V(n) asm volatile("s_waitcnt vmcnt(" #n ")" ::: "memory")
; #define G8_WAIT_L(n) asm volatile("s_waitcnt lgkmcnt(" #n ")" ::: "memory")
; #define G8_BAR __builtin_amdgcn_s_barrier()
; #define G8_SCHED __builtin_amdgcn_sched_barrier(0)
; template <class Epi, class Sched, int NT, bool F8 = false>
; __device__ __forceinline__ void gemm_phase(LAS unsigned char* lds, const Sched& S, const Epi& E) {
;     ...
;             G8_WAIT_V(8); G8_WAIT_L(0); G8_BAR; G8_MMA(1, 0, At, B0); G8_MMA(1, 1, At, B1); G8_BAR; G8_SCHED;
;         }
;         if (wr == 0) G8_BAR;
.LwDe:
	s_waitcnt lgkmcnt(0)
	s_barrier
	s_setprio 1
	s_waitcnt lgkmcnt(0)
	v_mfma_scale_f32_16x16x128_f8f6f4 v[126:129], v[2:9], v[34:41], v[126:129], v227, v227 op_sel_hi:[0,0,0]
	v_mfma_scale_f32_16x16x128_f8f6f4 v[122:125], v[10:17], v[34:41], v[122:125], v227, v227 op_sel_hi:[0,0,0]
	v_mfma_scale_f32_16x16x128_f8f6f4 v[114:117], v[2:9], v[42:49], v[114:117], v227, v227 op_sel_hi:[0,0,0]
	v_mfma_scale_f32_16x16x128_f8f6f4 v[106:109], v[10:17], v[42:49], v[106:109], v227, v227 op_sel_hi:[0,0,0]
	v_mfma_scale_f32_16x16x128_f8f6f4 v[98:101], v[2:9], v[50:57], v[98:101], v227, v227 op_sel_hi:[0,0,0]
	v_mfma_scale_f32_16x16x128_f8f6f4 v[90:93], v[10:17], v[50:57], v[90:93], v227, v227 op_sel_hi:[0,0,0]
	v_mfma_scale_f32_16x16x128_f8f6f4 v[82:85], v[2:9], v[58:65], v[82:85], v227, v227 op_sel_hi:[0,0,0]
	v_mfma_scale_f32_16x16x128_f8f6f4 v[74:77], v[10:17], v[58:65], v[74:77], v227, v227 op_sel_hi:[0,0,0]
	s_setprio 0
	s_setprio 1
	v_mfma_scale_f32_16x16x128_f8f6f4 v[118:121], v[18:25], v[34:41], v[118:121], v227, v227 op_sel_hi:[0,0,0]
	v_mfma_scale_f32_16x16x128_f8f6f4 v[110:113], v[26:33], v[34:41], v[110:113], v227, v227 op_sel_hi:[0,0,0]
	v_mfma_scale_f32_16x16x128_f8f6f4 v[102:105], v[18:25], v[42:49], v[102:105], v227, v227 op_sel_hi:[0,0,0]
	v_mfma_scale_f32_16x16x128_f8f6f4 v[94:97], v[26:33], v[42:49], v[94:97], v227, v227 op_sel_hi:[0,0,0]
	v_mfma_scale_f32_16x16x128_f8f6f4 v[86:89], v[18:25], v[50:57], v[86:89], v227, v227 op_sel_hi:[0,0,0]
	v_mfma_scale_f32_16x16x128_f8f6f4 v[78:81], v[26:33], v[50:57], v[78:81], v227, v227 op_sel_hi:[0,0,0]
	v_mfma_scale_f32_16x16x128_f8f6f4 v[70:73], v[18:25], v[58:65], v[70:73], v227, v227 op_sel_hi:[0,0,0]
	v_mfma_scale_f32_16x16x128_f8f6f4 v[66:69], v[26:33], v[58:65], v[66:69], v227, v227 op_sel_hi:[0,0,0]
	s_setprio 0
	s_barrier
	s_mov_b32 s13, 2
	s_mov_b64 s[30:31], 0
	s_mov_b64 s[28:29], -1
	s_and_b64 vcc, exec, s[26:27]
	s_cbranch_vccnz .LBB0_948
	.p2align 6

; #define LAS __attribute__((address_space(3)))
; __device__ __forceinline__ unsigned ld_agent(const unsigned* p) { return __hip_atomic_load(p, __ATOMIC_RELAXED, __HIP_MEMORY_SCOPE_AGENT); }
; __device__ __forceinline__ void p10_final(Ctx& F, bool have_tables) {
;     ...
;     __syncthreads();
;     if (have_tables) { if (F.tid < NE) ps[F.tid] = moe_tables(F).tp[F.tid] * 256; }
;     else { if (F.tid < NE) ps[64 + F.tid] = (((int)ld_agent(cnt + 32 * F.tid) + 255) >> 8) << 8;
;         __syncthreads();
;         if (F.tid < NE) { int acc = 0; for (int e = 0; e < F.tid; ++e) acc += ps[64 + e]; ps[F.tid] = acc; } }
;     __syncthreads();
;     LAS float* rowb = (LAS float*)(F.lds + 4096 + F.wave * 8192);
;     f32x4 gfv[4][2];
; #pragma unroll
;     for (int j = 0; j < 4; ++j)
; #pragma unroll
;         for (int hh = 0; hh < 2; ++hh) gfv[j][hh] = *(const f32x4*)(gf + 8 * lane + 512 * j + 4 * hh);
;     for (int t = gw; t < T; t += NGW) { const int b = t / SEQ; const float* gt2 = (const float*)(F.ws + WS_MOD) + (size_t)b * 6 * DM + 5 * DM;
;         int rows[9]; float wk[9];
;         { const i32x4 e0 = *(const i32x4*)(eidx + t * 8), e1 = *(const i32x4*)(eidx + t * 8 + 4), s0 = *(const i32x4*)(slot + t * 8), s1 = *(const i32x4*)(slot + t * 8 + 4);
.LBB0_1035:
	s_and_saveexec_b64 s[0:1], s[6:7]
	ds_write_b32 v1, v2
	s_or_b64 exec, exec, s[0:1]
	s_lshl_b32 s0, s85, 3
	s_add_i32 s0, s0, s67
	s_cmpk_gt_i32 s0, 0x3fff
	s_waitcnt lgkmcnt(0)
	s_barrier
	s_cbranch_scc1 .LBB0_1040
	v_readlane_b32 s8, v253, 0
	v_mov_b32_e32 v65, 0
	v_lshlrev_b32_e32 v64, 5, v230
	v_readlane_b32 s9, v253, 1
	s_movk_i32 s17, 0x1000
	s_mov_b64 s[2:3], 0x1000
	v_lshl_add_u64 v[16:17], s[8:9], 0, v[64:65]
	v_add_co_u32_e32 v36, vcc, s17, v16
	v_lshl_add_u64 v[32:33], v[16:17], 0, s[2:3]
	s_mov_b64 s[2:3], 0x1800
	v_addc_co_u32_e32 v37, vcc, 0, v17, vcc
	v_lshl_add_u64 v[34:35], v[16:17], 0, s[2:3]
	global_load_dwordx4 v[0:3], v64, s[8:9] offset:16
	global_load_dwordx4 v[4:7], v64, s[8:9]
	global_load_dwordx4 v[8:11], v64, s[8:9] offset:2064
	global_load_dwordx4 v[12:15], v64, s[8:9] offset:2048
	global_load_dwordx4 v[16:19], v[36:37], off
	global_load_dwordx4 v[20:23], v[36:37], off offset:2048
	global_load_dwordx4 v[24:27], v[32:33], off offset:16
	global_load_dwordx4 v[28:31], v[34:35], off offset:16
	s_lshl_b32 s2, s84, 3
	s_add_u32 s4, s96, 0x31a00000
	v_lshlrev_b32_e32 v32, 3, v230
	v_mov_b32_e32 v33, v65
	s_addc_u32 s5, s97, 0
	v_lshl_add_u64 v[68:69], s[4:5], 0, v[32:33]
	v_mbcnt_lo_u32_b32 v33, -1, 0
	v_mbcnt_hi_u32_b32 v33, -1, v33
	v_and_b32_e32 v35, 64, v33
	v_add_u32_e32 v35, 64, v35
	v_xor_b32_e32 v36, 1, v33
	v_cmp_lt_i32_e32 vcc, v36, v35
	s_add_u32 s18, s96, 0x27400000
	s_addc_u32 s19, s97, 0
	v_cndmask_b32_e32 v36, v33, v36, vcc
	v_lshlrev_b32_e32 v113, 2, v36
	v_xor_b32_e32 v36, 2, v33
	v_cmp_lt_i32_e32 vcc, v36, v35
	s_add_u32 s20, s96, 0x27500000
	s_addc_u32 s21, s97, 0
	v_cndmask_b32_e32 v36, v33, v36, vcc
	v_lshlrev_b32_e32 v115, 2, v36
	v_xor_b32_e32 v36, 4, v33
	v_cmp_lt_i32_e32 vcc, v36, v35
	s_add_u32 s22, s96, 0x27480000
	s_addc_u32 s23, s97, 0
	v_cndmask_b32_e32 v36, v33, v36, vcc
	v_lshlrev_b32_e32 v141, 2, v36
	v_xor_b32_e32 v36, 8, v33
	s_lshl_b32 s1, s67, 13
	v_cmp_lt_i32_e32 vcc, v36, v35
	s_add_i32 s1, s1, 0
	v_add_u32_e32 v111, s1, v64
	v_cndmask_b32_e32 v36, v33, v36, vcc
	v_lshlrev_b32_e32 v143, 2, v36
	v_xor_b32_e32 v36, 16, v33
	s_ashr_i32 s1, s0, 31
	v_readlane_b32 s10, v253, 2
	v_cmp_lt_i32_e32 vcc, v36, v35
	s_lshl_b64 s[6:7], s[0:1], 13
	v_readlane_b32 s11, v253, 3
	v_cndmask_b32_e32 v36, v33, v36, vcc
	s_add_u32 s6, s10, s6
	v_lshlrev_b32_e32 v144, 2, v36
	v_xor_b32_e32 v36, 32, v33
	s_addc_u32 s7, s11, s7
	s_ashr_i32 s3, s2, 31
	s_lshl_b32 s10, s85, 6
	s_lshl_b32 s11, s67, 3
	v_lshlrev_b32_e32 v66, 4, v230
	v_cmp_lt_i32_e32 vcc, v36, v35
	s_lshl_b64 s[8:9], s[2:3], 13
	s_add_i32 s10, s10, s11
	s_lshl_b32 s24, s84, 6
	s_lshl_b64 s[12:13], s[0:1], 12
	v_sub_u32_e32 v34, 0, v66
	v_or_b32_e32 v64, 0x200, v32
	v_or_b32_e32 v70, 0x400, v32
	v_or_b32_e32 v72, 0x600, v32
	v_cndmask_b32_e32 v33, v33, v36, vcc
	s_add_u32 s12, s96, s12
	v_mov_b32_e32 v71, v65
	v_mov_b32_e32 v73, v65
	v_lshlrev_b32_e32 v145, 2, v33
	v_mov_b32_e32 v67, v65
	s_addc_u32 s13, s97, s13
	s_lshl_b64 s[14:15], s[2:3], 12
	s_mov_b32 s16, 0x3d000000
	s_mov_b32 s1, 0x1f400000
	v_lshlrev_b32_e32 v146, 2, v32
	v_lshlrev_b32_e32 v147, 2, v64
	v_lshlrev_b32_e32 v148, 2, v70
	v_lshlrev_b32_e32 v149, 2, v72
	v_mov_b32_e32 v150, 0x358637bd
	s_mov_b32 s3, 0x800000
	v_add_u32_e32 v151, v111, v34
	.p2align 6
